# baseline (speedup 1.0000x reference)
.Lagg_scatter_done:
	v_and_b32_e32 v40, 1, v0
	v_cmp_eq_u32_e32 vcc, 0, v40
	s_movk_i32 s52, 0xc4
	v_cmp_gt_u32_e64 s[60:61], s52, v2
	s_and_b64 vcc, vcc, s[60:61]
	s_and_saveexec_b64 s[60:61], vcc
	v_bfe_u32 v40, v0, 1, 1
	v_mul_u32_u24_e32 v40, 0x310, v40
	v_lshl_add_u32 v40, v2, 2, v40
	ds_write_b32 v40, v3 offset:21248
	ds_write_b32 v40, v4 offset:22816
	s_mov_b64 exec, s[60:61]
	s_waitcnt vmcnt(0) lgkmcnt(0)
	s_barrier
	v_lshrrev_b32_e32 v40, 6, v0
	s_nop 0
	v_readfirstlane_b32 s41, v40
	s_cmp_gt_u32 s41, 13
	s_cbranch_scc1 .Lagg_exit
	v_mov_b32_e32 v15, 1.0
	s_lshl_b32 s52, s3, 8
	s_add_u32 s68, s30, s52
	s_addc_u32 s69, s31, 0
	s_mul_i32 s52, s3, 0x61a800
	s_add_u32 s70, s14, s52
	s_addc_u32 s71, s15, 0
	s_mul_i32 s52, s3, 0x61a800
	s_add_u32 s48, s12, s52
	s_addc_u32 s49, s13, 0
	s_lshl_b32 s52, s3, 7
	s_add_u32 s52, s18, s52
	s_addc_u32 s53, s19, 0
	v_lshlrev_b32_e32 v40, 1, v1
	global_load_dwordx4 v[16:19], v40, s[52:53]
	global_load_dwordx4 v[20:23], v40, s[52:53] offset:16
	global_load_dword v56, v13, s[20:21] offset:0
	global_load_dword v57, v13, s[20:21] offset:16
	s_waitcnt vmcnt(0)
	v_not_b32_e32 v58, v56
	v_and_b32_e32 v59, 0x7fffffff, v56
	v_cmp_gt_i32_e32 vcc, 0, v56
	s_nop 1
	v_cndmask_b32_e32 v56, v58, v59, vcc
	v_not_b32_e32 v58, v57
	v_and_b32_e32 v59, 0x7fffffff, v57
	v_cmp_gt_i32_e32 vcc, 0, v57
	s_nop 1
	v_cndmask_b32_e32 v57, v58, v59, vcc
	v_mov_b32_e32 v46, v56
	v_add_f32_e32 v14, v56, v57
	v_mul_f32_e32 v58, 0x3c23d70a, v14
	v_max_f32_e32 v14, v14, v58
	s_cmp_eq_u32 s7, 0
	s_cbranch_scc1 .Lagg_slow_0
	s_lshl_b32 s40, s41, 4
	s_cmp_eq_u32 s40, 0xc0
	s_cselect_b32 s40, 0xd0, s40
	s_cmp_eq_u32 s41, 13
	s_cselect_b32 s40, 0xc0, s40
	v_bfe_u32 v63, v0, 2, 4
	v_add_u32_e32 v63, s40, v63
	v_cmp_gt_u32_e32 vcc, 0xc4, v63
	s_and_saveexec_b64 s[58:59], vcc
	s_cbranch_execz .Lagg_phasedone_0_0
	v_lshlrev_b32_e32 v63, 1, v63
	ds_read_u16 v60, v63 offset:18432
	v_lshrrev_b32_e32 v63, 2, v1
	s_waitcnt lgkmcnt(0)
	v_lshlrev_b32_e32 v61, 2, v60
	ds_read_b32 v58, v61 offset:14336
	ds_read_b32 v59, v61 offset:14340
	v_bfe_u32 v57, v0, 1, 1
	v_mul_u32_u24_e32 v57, 0x310, v57
	v_lshl_add_u32 v57, v60, 2, v57
	ds_read_b32 v57, v57 offset:21248
	v_lshl_add_u32 v61, v60, 4, v63
	v_mov_b32_e32 v45, 0
	v_mov_b32_e32 v48, 0
	v_mov_b32_e32 v49, 0
	v_mov_b32_e32 v50, 0
	v_mov_b32_e32 v51, 0
	v_mov_b32_e32 v52, 0
	v_mov_b32_e32 v53, 0
	v_mov_b32_e32 v54, 0
	v_mov_b32_e32 v55, 0
	s_waitcnt lgkmcnt(0)
	v_lshlrev_b32_e32 v41, 1, v58
	v_lshlrev_b32_e32 v42, 1, v59
	v_cmp_lt_u32_e32 vcc, v41, v42
	s_and_saveexec_b64 s[64:65], vcc
	s_cbranch_execz .Lagg_listdone_0_0
	ds_read_u16 v40, v41
	v_add_u32_e32 v41, 2, v41
	s_waitcnt lgkmcnt(0)
	v_mad_u32_u16 v24, v40, s46, v1
	global_load_dwordx4 v[28:31], v24, s[48:49] offset:64
	global_load_dwordx4 v[24:27], v24, s[48:49]
	s_waitcnt lgkmcnt(0)
	v_add_f32_e32 v47, v46, v57
	v_mul_f32_e32 v56, 0x3c23d70a, v47
	v_max_f32_e32 v47, v47, v56
	v_sub_f32_e32 v43, v57, v47
	v_mul_f32_e32 v43, 0.5, v43
	v_mul_f32_e32 v44, 0xbf7d70a4, v47

.Lagg_phasedone_0_0:
	s_mov_b64 exec, s[58:59]
	s_sub_u32 s40, 12, s41
	s_lshl_b32 s40, s40, 4
	s_cmp_eq_u32 s40, 0xc0
	s_cselect_b32 s40, 0xd0, s40
	s_cmp_eq_u32 s41, 13
	s_cselect_b32 s40, 0xc0, s40
	v_bfe_u32 v63, v0, 2, 4
	v_add_u32_e32 v63, s40, v63
	v_cmp_gt_u32_e32 vcc, 0xc4, v63
	s_and_saveexec_b64 s[58:59], vcc
	s_cbranch_execz .Lagg_phasedone_0_1
	v_lshlrev_b32_e32 v63, 1, v63
	ds_read_u16 v60, v63 offset:18824
	v_lshrrev_b32_e32 v63, 2, v1
	s_waitcnt lgkmcnt(0)
	v_lshlrev_b32_e32 v61, 2, v60
	ds_read_b32 v58, v61 offset:15120
	ds_read_b32 v59, v61 offset:15124
	v_bfe_u32 v57, v0, 1, 1
	v_mul_u32_u24_e32 v57, 0x310, v57
	v_lshl_add_u32 v57, v60, 2, v57
	ds_read_b32 v57, v57 offset:21248
	v_lshl_add_u32 v61, v60, 4, v63
	v_add_u32_e32 v61, 0x6e40, v61
	v_mov_b32_e32 v45, 0
	v_mov_b32_e32 v48, 0
	v_mov_b32_e32 v49, 0
	v_mov_b32_e32 v50, 0
	v_mov_b32_e32 v51, 0
	v_mov_b32_e32 v52, 0
	v_mov_b32_e32 v53, 0
	v_mov_b32_e32 v54, 0
	v_mov_b32_e32 v55, 0
	s_waitcnt lgkmcnt(0)
	v_lshlrev_b32_e32 v41, 1, v58
	v_lshlrev_b32_e32 v42, 1, v59
	v_cmp_lt_u32_e32 vcc, v41, v42
	s_and_saveexec_b64 s[64:65], vcc
	s_cbranch_execz .Lagg_listdone_0_1
	ds_read_u16 v40, v41
	v_add_u32_e32 v41, 2, v41
	s_waitcnt lgkmcnt(0)
	v_mad_u32_u16 v24, v40, s46, v1
	global_load_dwordx4 v[28:31], v24, s[48:49] offset:64
	global_load_dwordx4 v[24:27], v24, s[48:49]
	s_waitcnt lgkmcnt(0)
	v_add_f32_e32 v47, v46, v57
	v_mul_f32_e32 v56, 0x3c23d70a, v47
	v_max_f32_e32 v47, v47, v56
	v_sub_f32_e32 v43, v57, v47
	v_mul_f32_e32 v43, 0.5, v43
	v_mul_f32_e32 v44, 0xbf7d70a4, v47

.Lagg_end_0:
	s_mov_b64 exec, s[58:59]
	s_mul_i32 s52, s3, 0x61a800
	s_add_u32 s52, s52, 0xc35000
	s_add_u32 s48, s12, s52
	s_addc_u32 s49, s13, 0
	s_lshl_b32 s52, s3, 7
	s_add_u32 s52, s52, 0x100
	s_add_u32 s52, s18, s52
	s_addc_u32 s53, s19, 0
	v_lshlrev_b32_e32 v40, 1, v1
	global_load_dwordx4 v[16:19], v40, s[52:53]
	global_load_dwordx4 v[20:23], v40, s[52:53] offset:16
	global_load_dword v56, v13, s[20:21] offset:32
	global_load_dword v57, v13, s[20:21] offset:48
	s_waitcnt vmcnt(0)
	v_not_b32_e32 v58, v56
	v_and_b32_e32 v59, 0x7fffffff, v56
	v_cmp_gt_i32_e32 vcc, 0, v56
	s_nop 1
	v_cndmask_b32_e32 v56, v58, v59, vcc
	v_not_b32_e32 v58, v57
	v_and_b32_e32 v59, 0x7fffffff, v57
	v_cmp_gt_i32_e32 vcc, 0, v57
	s_nop 1
	v_cndmask_b32_e32 v57, v58, v59, vcc
	v_mov_b32_e32 v46, v56
	v_add_f32_e32 v14, v56, v57
	v_mul_f32_e32 v58, 0x3c23d70a, v14
	v_max_f32_e32 v14, v14, v58
	s_cmp_eq_u32 s7, 0
	s_cbranch_scc1 .Lagg_slow_1
	s_sub_u32 s40, 12, s41
	s_lshl_b32 s40, s40, 4
	s_cmp_eq_u32 s40, 0xc0
	s_cselect_b32 s40, 0xd0, s40
	s_cmp_eq_u32 s41, 13
	s_cselect_b32 s40, 0xc0, s40
	v_bfe_u32 v63, v0, 2, 4
	v_add_u32_e32 v63, s40, v63
	v_cmp_gt_u32_e32 vcc, 0xc4, v63
	s_and_saveexec_b64 s[58:59], vcc
	s_cbranch_execz .Lagg_phasedone_1_0
	v_lshlrev_b32_e32 v63, 1, v63
	ds_read_u16 v60, v63 offset:19216
	v_lshrrev_b32_e32 v63, 2, v1
	s_waitcnt lgkmcnt(0)
	v_lshlrev_b32_e32 v61, 2, v60
	ds_read_b32 v58, v61 offset:16384
	ds_read_b32 v59, v61 offset:16388
	v_bfe_u32 v57, v0, 1, 1
	v_mul_u32_u24_e32 v57, 0x310, v57
	v_lshl_add_u32 v57, v60, 2, v57
	ds_read_b32 v57, v57 offset:22816
	v_lshl_add_u32 v61, v60, 4, v63
	v_mov_b32_e32 v45, 0
	v_mov_b32_e32 v48, 0
	v_mov_b32_e32 v49, 0
	v_mov_b32_e32 v50, 0
	v_mov_b32_e32 v51, 0
	v_mov_b32_e32 v52, 0
	v_mov_b32_e32 v53, 0
	v_mov_b32_e32 v54, 0
	v_mov_b32_e32 v55, 0
	s_waitcnt lgkmcnt(0)
	v_lshlrev_b32_e32 v41, 1, v58
	v_lshlrev_b32_e32 v42, 1, v59
	v_add_u32_e32 v41, 0x1c00, v41
	v_add_u32_e32 v42, 0x1c00, v42
	v_cmp_lt_u32_e32 vcc, v41, v42
	s_and_saveexec_b64 s[64:65], vcc
	s_cbranch_execz .Lagg_listdone_1_0
	ds_read_u16 v40, v41
	v_add_u32_e32 v41, 2, v41
	s_waitcnt lgkmcnt(0)
	v_mad_u32_u16 v24, v40, s46, v1
	global_load_dwordx4 v[28:31], v24, s[48:49] offset:64
	global_load_dwordx4 v[24:27], v24, s[48:49]
	s_waitcnt lgkmcnt(0)
	v_add_f32_e32 v47, v46, v57
	v_mul_f32_e32 v56, 0x3c23d70a, v47
	v_max_f32_e32 v47, v47, v56
	v_sub_f32_e32 v43, v57, v47
	v_mul_f32_e32 v43, 0.5, v43
	v_mul_f32_e32 v44, 0xbf7d70a4, v47

.Lagg_phasedone_1_0:
	s_mov_b64 exec, s[58:59]
	s_lshl_b32 s40, s41, 4
	s_cmp_eq_u32 s40, 0xc0
	s_cselect_b32 s40, 0xd0, s40
	s_cmp_eq_u32 s41, 13
	s_cselect_b32 s40, 0xc0, s40
	v_bfe_u32 v63, v0, 2, 4
	v_add_u32_e32 v63, s40, v63
	v_cmp_gt_u32_e32 vcc, 0xc4, v63
	s_and_saveexec_b64 s[58:59], vcc
	s_cbranch_execz .Lagg_phasedone_1_1
	v_lshlrev_b32_e32 v63, 1, v63
	ds_read_u16 v60, v63 offset:19608
	v_lshrrev_b32_e32 v63, 2, v1
	s_waitcnt lgkmcnt(0)
	v_lshlrev_b32_e32 v61, 2, v60
	ds_read_b32 v58, v61 offset:17168
	ds_read_b32 v59, v61 offset:17172
	v_bfe_u32 v57, v0, 1, 1
	v_mul_u32_u24_e32 v57, 0x310, v57
	v_lshl_add_u32 v57, v60, 2, v57
	ds_read_b32 v57, v57 offset:22816
	v_lshl_add_u32 v61, v60, 4, v63
	v_add_u32_e32 v61, 0x6e40, v61
	v_mov_b32_e32 v45, 0
	v_mov_b32_e32 v48, 0
	v_mov_b32_e32 v49, 0
	v_mov_b32_e32 v50, 0
	v_mov_b32_e32 v51, 0
	v_mov_b32_e32 v52, 0
	v_mov_b32_e32 v53, 0
	v_mov_b32_e32 v54, 0
	v_mov_b32_e32 v55, 0
	s_waitcnt lgkmcnt(0)
	v_lshlrev_b32_e32 v41, 1, v58
	v_lshlrev_b32_e32 v42, 1, v59
	v_add_u32_e32 v41, 0x1c00, v41
	v_add_u32_e32 v42, 0x1c00, v42
	v_cmp_lt_u32_e32 vcc, v41, v42
	s_and_saveexec_b64 s[64:65], vcc
	s_cbranch_execz .Lagg_listdone_1_1
	ds_read_u16 v40, v41
	v_add_u32_e32 v41, 2, v41
	s_waitcnt lgkmcnt(0)
	v_mad_u32_u16 v24, v40, s46, v1
	global_load_dwordx4 v[28:31], v24, s[48:49] offset:64
	global_load_dwordx4 v[24:27], v24, s[48:49]
	s_waitcnt lgkmcnt(0)
	v_add_f32_e32 v47, v46, v57
	v_mul_f32_e32 v56, 0x3c23d70a, v47
	v_max_f32_e32 v47, v47, v56
	v_sub_f32_e32 v43, v57, v47
	v_mul_f32_e32 v43, 0.5, v43
	v_mul_f32_e32 v44, 0xbf7d70a4, v47
